# v038 + both MoE down-projection phases process each XCD's odd expert first (its HID was written last by the preceding gate/up phase: infinity-cache residency)
# speedup vs baseline: 1.0130x; 1.0130x over previous
;     __device__ bool next(int i, Unit& u) const { return map((long)i * G + c, u); }
;     __device__ bool next(int i, Unit& u) const { if (!p.next(i, u)) return false; if (u.pn >= 4) u.pn += 2; return true; }
;     __device__ bool next(int i, Unit& u) const { const int L = i * G + c; if (L >= 4 * 66) return false; const int wi = L / 66; u.kq = -1; u.z = 0; u.pm = wi < 2 ? 4 + wi : 6 + wi; u.pn = L % 66; return true; }
;     __device__ bool next(int i, Unit& u) const { if (!p.next(i, u)) return false; if (u.pn >= 4) u.pn += 12; return true; }
;     __device__ bool next(int i, Unit& u) const { const int L = i * G + c; if (L >= total) return false; u.kq = -1; u.z = 0; u.pm = wt0 + L / nTok; u.pn = tok0 + L % nTok; return true; }
;     __device__ bool next(int i, Unit& u) const { if (i > 0 || c >= 48) return false; const int t = c >> 1; u.kq = c & 1; u.z = 0; u.pm = 4 + (t >> 1); u.pn = 64 + (t & 1); return true; }
;     __device__ bool next(int i, Unit& u) const {
;         const int x = c & 7, j = (c >> 3) + i * (G >> 3);
;         if (j >= 96) return false;
;         const int g = j / 12, k = j - 12 * g;
;         u.z = 2 * x + (g >> 2); u.pn = g & 3;
;         if (k < 8) { u.kq = -1; u.pm = k; } else { u.kq = k - 8; u.pm = 8; }
;         return true;
;     }
.LBB0_1074:
	s_or_b64 exec, exec, s[0:1]
	v_mov_b32_e32 v3, v0
	s_cmpk_lt_i32 s75, 0x60
	s_waitcnt lgkmcnt(0)
	s_barrier
	s_cselect_b64 s[0:1], -1, 0
	s_cmpk_gt_i32 s75, 0x5f
	v_readfirstlane_b32 s10, v3
	s_cbranch_scc1 .LBB0_1076
	s_mul_hi_i32 s2, s75, 0x2aaaaaab
	s_lshr_b32 s3, s2, 31
	s_ashr_i32 s2, s2, 1
	s_add_i32 s2, s2, s3
	s_mul_i32 s3, s2, -12
	s_add_i32 s3, s3, s75
	s_lshl_b32 s4, s94, 1
	s_and_b32 s4, s4, 14
	s_ashr_i32 s5, s2, 2
	s_and_b32 s56, s2, 3
	s_max_i32 s2, s3, 7
	s_add_i32 s57, s5, s4
	s_xor_b32 s57, s57, 1
	s_add_i32 s45, s2, -8
	s_min_i32 s58, s3, 8

;     __device__ bool next(int i, Unit& u) const { return map((long)i * G + c, u); }
;     __device__ bool next(int i, Unit& u) const { if (!p.next(i, u)) return false; if (u.pn >= 4) u.pn += 2; return true; }
;     __device__ bool next(int i, Unit& u) const { const int L = i * G + c; if (L >= 4 * 66) return false; const int wi = L / 66; u.kq = -1; u.z = 0; u.pm = wi < 2 ? 4 + wi : 6 + wi; u.pn = L % 66; return true; }
;     __device__ bool next(int i, Unit& u) const { if (!p.next(i, u)) return false; if (u.pn >= 4) u.pn += 12; return true; }
;     __device__ bool next(int i, Unit& u) const { const int L = i * G + c; if (L >= total) return false; u.kq = -1; u.z = 0; u.pm = wt0 + L / nTok; u.pn = tok0 + L % nTok; return true; }
;     __device__ bool next(int i, Unit& u) const { if (i > 0 || c >= 48) return false; const int t = c >> 1; u.kq = c & 1; u.z = 0; u.pm = 4 + (t >> 1); u.pn = 64 + (t & 1); return true; }
;     __device__ bool next(int i, Unit& u) const {
;         const int x = c & 7, j = (c >> 3) + i * (G >> 3);
;         if (j >= 96) return false;
;         const int g = j / 12, k = j - 12 * g;
;         u.z = 2 * x + (g >> 2); u.pn = g & 3;
;         if (k < 8) { u.kq = -1; u.pm = k; } else { u.kq = k - 8; u.pm = 8; }
;         return true;
;     }
.LBB0_1086:
	s_add_i32 s38, s38, 1
	s_mul_i32 s0, s38, s46
	s_add_i32 s0, s0, s75
	s_cmpk_lt_i32 s0, 0x60
	s_cselect_b64 s[4:5], -1, 0
	s_cmpk_gt_i32 s0, 0x5f
	s_cbranch_scc1 .LBB0_1088
	s_mul_hi_i32 s1, s0, 0x2aaaaaab
	s_lshr_b32 s14, s1, 31
	s_ashr_i32 s1, s1, 1
	s_add_i32 s1, s1, s14
	s_mul_i32 s14, s1, -12
	s_add_i32 s14, s14, s0
	s_ashr_i32 s0, s1, 2
	s_add_i32 s54, s0, s47
	s_xor_b32 s54, s54, 1
	s_max_i32 s0, s14, 7
	s_and_b32 s52, s1, 3
	s_add_i32 s53, s0, -8
	s_min_i32 s55, s14, 8
